# baseline (speedup 1.0000x reference)
_Z8k_expertPKDF16_S0_PKfPcPiS0_S2_S2_S2_S2_PfS5_S4_S2_S2_S2_S2_S5_S2_S2_S2_:
	s_lshl_b32 s3, s2, 2
	s_load_dwordx8 s[8:15], s[0:1], 0x88
	s_load_dwordx2 s[70:71], s[0:1], 0x0
	s_and_b32 s3, s3, 28
	s_ashr_i32 s4, s2, 6
	s_add_i32 s34, s3, s4
	s_ashr_i32 s6, s34, 1
	v_mov_b32_e32 v2, v0
	s_lshl_b32 s4, s6, 4
	s_ashr_i32 s5, s4, 31
	v_ashrrev_i32_e32 v3, 31, v2
	s_waitcnt lgkmcnt(0)
	v_lshl_add_u64 v[4:5], v[2:3], 2, s[10:11]
	s_lshl_b64 s[10:11], s[4:5], 11
	v_lshl_add_u64 v[6:7], v[4:5], 0, s[10:11]
	s_or_b32 s10, s4, 1
	s_ashr_i32 s11, s10, 31
	s_lshl_b64 s[10:11], s[10:11], 11
	v_lshl_add_u64 v[8:9], v[4:5], 0, s[10:11]
	s_or_b32 s10, s4, 2
	s_ashr_i32 s11, s10, 31
	s_lshl_b64 s[10:11], s[10:11], 11
	v_lshl_add_u64 v[10:11], v[4:5], 0, s[10:11]
	s_or_b32 s10, s4, 3
	s_ashr_i32 s11, s10, 31
	s_lshl_b64 s[10:11], s[10:11], 11
	v_lshl_add_u64 v[12:13], v[4:5], 0, s[10:11]
	s_or_b32 s10, s4, 4
	s_ashr_i32 s11, s10, 31
	s_lshl_b64 s[10:11], s[10:11], 11
	v_lshl_add_u64 v[14:15], v[4:5], 0, s[10:11]
	s_or_b32 s10, s4, 5
	s_ashr_i32 s11, s10, 31
	s_lshl_b64 s[10:11], s[10:11], 11
	v_lshl_add_u64 v[16:17], v[4:5], 0, s[10:11]
	s_or_b32 s10, s4, 6
	s_ashr_i32 s11, s10, 31
	s_lshl_b64 s[10:11], s[10:11], 11
	v_lshl_add_u64 v[18:19], v[4:5], 0, s[10:11]
	s_or_b32 s10, s4, 7
	s_ashr_i32 s11, s10, 31
	s_lshl_b64 s[10:11], s[10:11], 11
	v_lshl_add_u64 v[20:21], v[4:5], 0, s[10:11]
	s_or_b32 s10, s4, 8
	s_ashr_i32 s11, s10, 31
	s_lshl_b64 s[10:11], s[10:11], 11
	global_load_dword v1, v[6:7], off
	global_load_dword v3, v[8:9], off
	global_load_dword v22, v[10:11], off
	global_load_dword v23, v[12:13], off
	global_load_dword v24, v[14:15], off
	global_load_dword v25, v[16:17], off
	global_load_dword v26, v[18:19], off
	global_load_dword v27, v[20:21], off
	v_lshl_add_u64 v[6:7], v[4:5], 0, s[10:11]
	s_or_b32 s10, s4, 9
	s_ashr_i32 s11, s10, 31
	s_lshl_b64 s[10:11], s[10:11], 11
	v_lshl_add_u64 v[8:9], v[4:5], 0, s[10:11]
	s_or_b32 s10, s4, 10
	s_ashr_i32 s11, s10, 31
	s_lshl_b64 s[10:11], s[10:11], 11
	v_lshl_add_u64 v[10:11], v[4:5], 0, s[10:11]
	s_or_b32 s10, s4, 11
	s_ashr_i32 s11, s10, 31
	s_lshl_b64 s[10:11], s[10:11], 11
	v_lshl_add_u64 v[12:13], v[4:5], 0, s[10:11]
	s_or_b32 s10, s4, 12
	s_ashr_i32 s11, s10, 31
	s_lshl_b64 s[10:11], s[10:11], 11
	v_lshl_add_u64 v[14:15], v[4:5], 0, s[10:11]
	s_or_b32 s10, s4, 13
	s_ashr_i32 s11, s10, 31
	s_lshl_b64 s[10:11], s[10:11], 11
	v_lshl_add_u64 v[16:17], v[4:5], 0, s[10:11]
	s_or_b32 s10, s4, 14
	s_or_b32 s4, s4, 15
	s_ashr_i32 s11, s10, 31
	s_ashr_i32 s5, s4, 31
	s_lshl_b64 s[10:11], s[10:11], 11
	s_lshl_b64 s[4:5], s[4:5], 11
	v_lshl_add_u64 v[18:19], v[4:5], 0, s[10:11]
	v_lshl_add_u64 v[4:5], v[4:5], 0, s[4:5]
	global_load_dword v20, v[6:7], off
	global_load_dword v21, v[8:9], off
	global_load_dword v28, v[10:11], off
	global_load_dword v29, v[12:13], off
	global_load_dword v30, v[14:15], off
	global_load_dword v31, v[16:17], off
	global_load_dword v32, v[18:19], off
	global_load_dword v33, v[4:5], off
	v_lshlrev_b32_e32 v4, 3, v2
	v_ashrrev_i32_e32 v5, 31, v4
	v_lshl_add_u64 v[12:13], v[4:5], 2, s[12:13]
	global_load_dwordx4 v[4:7], v[12:13], off
	global_load_dwordx4 v[8:11], v[12:13], off offset:16
	v_and_b32_e32 v200, 63, v0
	v_lshrrev_b32_e32 v201, 6, v0
	v_lshlrev_b32_e32 v202, 4, v200
	v_and_b32_e32 v203, 32, v200
	v_xor_b32_e32 v202, v202, v203
	v_lshrrev_b32_e32 v203, 6, v202
	v_lshrrev_b32_e32 v204, 1, v201
	v_lshl_add_u32 v203, v204, 4, v203
	v_and_b32_e32 v204, 62, v202
	v_and_b32_e32 v205, 1, v201
	v_lshl_add_u32 v204, v205, 6, v204
	v_lshl_add_u32 v200, v203, 12, v204
	v_add_u32_e32 v201, 0x40000, v200
	s_lshl_b32 s72, s6, 22
	s_lshr_b32 s73, s2, 4
	s_and_b32 s73, s73, 3
	s_lshl_b32 s73, s73, 20
	s_add_u32 s72, s72, s73
	s_lshl_b32 s81, s6, 8
	s_add_u32 s72, s72, s81
	s_add_u32 s83, s81, 0x80
	s_and_b32 s83, s83, 0xfff
	s_or_b32 s82, s83, 0x80000
	s_add_u32 s88, s81, 0xf80
	s_and_b32 s88, s88, 0xfff
	s_or_b32 s88, s88, 0x80000
	s_add_u32 s74, s70, s72
	s_addc_u32 s75, s71, 0
	s_add_u32 s76, s74, 0x80000
	s_addc_u32 s77, s75, 0
	v_readfirstlane_b32 s78, v0
	s_lshl_b32 s78, s78, 4
	s_mov_b32 m0, s78
	s_add_i32 s79, s78, 0x2000
	global_load_lds_dwordx4 v200, s[74:75]
	s_mov_b32 m0, s79
	s_add_i32 s79, s78, 0x4000
	global_load_lds_dwordx4 v201, s[74:75]
	s_mov_b32 m0, s79
	s_add_i32 s79, s78, 0x6000
	global_load_lds_dwordx4 v200, s[76:77]
	s_mov_b32 m0, s79
	s_nop 0
	global_load_lds_dwordx4 v201, s[76:77]
	s_waitcnt vmcnt(21)
	v_add_f32_e32 v1, 0, v1
	s_waitcnt vmcnt(20)
	v_add_f32_e32 v1, v1, v3
	s_waitcnt vmcnt(19)
	v_add_f32_e32 v1, v1, v22
	s_waitcnt vmcnt(18)
	v_add_f32_e32 v1, v1, v23
	s_waitcnt vmcnt(17)
	v_add_f32_e32 v1, v1, v24
	s_waitcnt vmcnt(16)
	v_add_f32_e32 v1, v1, v25
	s_waitcnt vmcnt(15)
	v_add_f32_e32 v1, v1, v26
	s_waitcnt vmcnt(14)
	v_add_f32_e32 v1, v1, v27
	s_waitcnt vmcnt(13)
	v_add_f32_e32 v1, v1, v20
	s_waitcnt vmcnt(12)
	v_add_f32_e32 v1, v1, v21
	s_waitcnt vmcnt(11)
	v_add_f32_e32 v1, v1, v28
	s_waitcnt vmcnt(10)
	v_add_f32_e32 v1, v1, v29
	s_waitcnt vmcnt(9)
	v_add_f32_e32 v1, v1, v30
	s_waitcnt vmcnt(8)
	v_add_f32_e32 v1, v1, v31
	s_waitcnt vmcnt(7)
	v_add_f32_e32 v1, v1, v32
	s_waitcnt vmcnt(6)
	v_add_f32_e32 v1, v1, v33
	v_mul_f32_e32 v12, 0x3a800000, v1
	v_mbcnt_lo_u32_b32 v1, -1, 0
	v_mbcnt_hi_u32_b32 v3, -1, v1
	v_xor_b32_e32 v13, 32, v3
	v_lshlrev_b32_e32 v183, 2, v13
	v_xor_b32_e32 v13, 16, v3
	v_lshlrev_b32_e32 v181, 2, v13
	v_xor_b32_e32 v13, 8, v3
	v_lshlrev_b32_e32 v1, 2, v13
	v_xor_b32_e32 v13, 4, v3
	v_lshlrev_b32_e32 v180, 2, v13
	v_xor_b32_e32 v13, 2, v3
	v_lshlrev_b32_e32 v182, 2, v13
	v_xor_b32_e32 v13, 1, v3
	v_lshlrev_b32_e32 v184, 2, v13
	v_cmp_eq_u32_e32 vcc, 0, v3
	v_mov_b32_e32 v13, v12
	s_waitcnt vmcnt(4)
	v_pk_mul_f32 v[14:15], v[12:13], v[4:5]
	v_pk_mul_f32 v[16:17], v[12:13], v[6:7]
	v_pk_mul_f32 v[18:19], v[12:13], v[8:9]
	v_pk_mul_f32 v[20:21], v[12:13], v[10:11]
	v_add_f32_dpp v14, v14, v14 quad_perm:[1,0,3,2] row_mask:0xf bank_mask:0xf
	v_add_f32_dpp v15, v15, v15 quad_perm:[1,0,3,2] row_mask:0xf bank_mask:0xf
	v_add_f32_dpp v16, v16, v16 quad_perm:[1,0,3,2] row_mask:0xf bank_mask:0xf
	v_add_f32_dpp v17, v17, v17 quad_perm:[1,0,3,2] row_mask:0xf bank_mask:0xf
	v_add_f32_dpp v18, v18, v18 quad_perm:[1,0,3,2] row_mask:0xf bank_mask:0xf
	v_add_f32_dpp v19, v19, v19 quad_perm:[1,0,3,2] row_mask:0xf bank_mask:0xf
	v_add_f32_dpp v20, v20, v20 quad_perm:[1,0,3,2] row_mask:0xf bank_mask:0xf
	v_add_f32_dpp v21, v21, v21 quad_perm:[1,0,3,2] row_mask:0xf bank_mask:0xf
	v_add_f32_dpp v14, v14, v14 quad_perm:[2,3,0,1] row_mask:0xf bank_mask:0xf
	v_add_f32_dpp v15, v15, v15 quad_perm:[2,3,0,1] row_mask:0xf bank_mask:0xf
	v_add_f32_dpp v16, v16, v16 quad_perm:[2,3,0,1] row_mask:0xf bank_mask:0xf
	v_add_f32_dpp v17, v17, v17 quad_perm:[2,3,0,1] row_mask:0xf bank_mask:0xf
	v_add_f32_dpp v18, v18, v18 quad_perm:[2,3,0,1] row_mask:0xf bank_mask:0xf
	v_add_f32_dpp v19, v19, v19 quad_perm:[2,3,0,1] row_mask:0xf bank_mask:0xf
	v_add_f32_dpp v20, v20, v20 quad_perm:[2,3,0,1] row_mask:0xf bank_mask:0xf
	v_add_f32_dpp v21, v21, v21 quad_perm:[2,3,0,1] row_mask:0xf bank_mask:0xf
	v_add_f32_dpp v14, v14, v14 row_half_mirror row_mask:0xf bank_mask:0xf
	v_add_f32_dpp v15, v15, v15 row_half_mirror row_mask:0xf bank_mask:0xf
	v_add_f32_dpp v16, v16, v16 row_half_mirror row_mask:0xf bank_mask:0xf
	v_add_f32_dpp v17, v17, v17 row_half_mirror row_mask:0xf bank_mask:0xf
	v_add_f32_dpp v18, v18, v18 row_half_mirror row_mask:0xf bank_mask:0xf
	v_add_f32_dpp v19, v19, v19 row_half_mirror row_mask:0xf bank_mask:0xf
	v_add_f32_dpp v20, v20, v20 row_half_mirror row_mask:0xf bank_mask:0xf
	v_add_f32_dpp v21, v21, v21 row_half_mirror row_mask:0xf bank_mask:0xf
	v_add_f32_dpp v14, v14, v14 row_mirror row_mask:0xf bank_mask:0xf
	v_add_f32_dpp v15, v15, v15 row_mirror row_mask:0xf bank_mask:0xf
	v_add_f32_dpp v16, v16, v16 row_mirror row_mask:0xf bank_mask:0xf
	v_add_f32_dpp v17, v17, v17 row_mirror row_mask:0xf bank_mask:0xf
	v_add_f32_dpp v18, v18, v18 row_mirror row_mask:0xf bank_mask:0xf
	v_add_f32_dpp v19, v19, v19 row_mirror row_mask:0xf bank_mask:0xf
	v_add_f32_dpp v20, v20, v20 row_mirror row_mask:0xf bank_mask:0xf
	v_add_f32_dpp v21, v21, v21 row_mirror row_mask:0xf bank_mask:0xf
	ds_bpermute_b32 v22, v181, v14
	ds_bpermute_b32 v23, v181, v15
	ds_bpermute_b32 v24, v181, v16
	ds_bpermute_b32 v25, v181, v17
	ds_bpermute_b32 v26, v181, v18
	ds_bpermute_b32 v27, v181, v19
	ds_bpermute_b32 v28, v181, v20
	ds_bpermute_b32 v29, v181, v21
	s_waitcnt lgkmcnt(0)
	v_pk_add_f32 v[14:15], v[14:15], v[22:23]
	v_pk_add_f32 v[16:17], v[16:17], v[24:25]
	v_pk_add_f32 v[18:19], v[18:19], v[26:27]
	v_pk_add_f32 v[20:21], v[20:21], v[28:29]
	ds_bpermute_b32 v22, v183, v14
	ds_bpermute_b32 v23, v183, v15
	ds_bpermute_b32 v24, v183, v16
	ds_bpermute_b32 v25, v183, v17
	ds_bpermute_b32 v26, v183, v18
	ds_bpermute_b32 v27, v183, v19
	ds_bpermute_b32 v28, v183, v20
	ds_bpermute_b32 v29, v183, v21
	s_waitcnt lgkmcnt(0)
	v_pk_add_f32 v[14:15], v[14:15], v[22:23]
	v_pk_add_f32 v[16:17], v[16:17], v[24:25]
	v_pk_add_f32 v[18:19], v[18:19], v[26:27]
	v_pk_add_f32 v[20:21], v[20:21], v[28:29]
	s_and_saveexec_b64 s[4:5], vcc
	s_cbranch_execz .LBB5_2
	v_lshrrev_b32_e32 v22, 1, v0
	v_add_u32_e32 v22, 0x20000, v22
	ds_write_b128 v22, v[14:17]
	ds_write_b128 v22, v[18:21] offset:16

.LBB5_6:
	s_or_b64 exec, exec, s[10:11]
	s_load_dwordx2 s[10:11], s[0:1], 0x80
	s_load_dwordx2 s[36:37], s[0:1], 0x70
	s_load_dwordx2 s[40:41], s[0:1], 0x60
	s_load_dwordx4 s[20:23], s[0:1], 0x50
	s_load_dwordx8 s[12:19], s[0:1], 0x30
	s_load_dwordx4 s[24:27], s[0:1], 0x10
	s_load_dwordx2 s[46:47], s[0:1], 0x20
	s_and_b32 s58, s59, 1
	s_cmp_eq_u32 s35, 0
	s_cselect_b32 s42, s3, s7
	s_ashr_i32 s7, s6, 31
	s_lshl_b64 s[52:53], s[6:7], 22
	s_waitcnt lgkmcnt(0)
	s_lshl_b32 s64, s42, 11
	s_lshl_b32 s65, s58, 10
	s_add_u32 s64, s64, s65
	s_add_u32 s66, s24, s64
	s_addc_u32 s67, s25, 0
	s_mov_b32 m0, 0x22240
	v_and_b32_e32 v254, 63, v0
	v_lshlrev_b32_e32 v254, 4, v254
	global_load_lds_dwordx4 v254, s[66:67]
	s_lshl_b32 s64, s42, 10
	s_add_u32 s66, s12, s64
	s_addc_u32 s67, s13, 0
	s_mov_b32 m0, 0x22640
	s_lshl_b32 s65, s42, 2
	global_load_lds_dwordx4 v254, s[66:67]
	s_add_u32 s66, s14, s64
	s_addc_u32 s67, s15, 0
	s_mov_b32 m0, 0x22a40
	s_nop 0
	global_load_lds_dwordx4 v254, s[66:67]
	s_add_u32 s66, s16, s64
	s_addc_u32 s67, s17, 0
	s_mov_b32 m0, 0x22e40
	s_load_dword s69, s[18:19], s65
	global_load_lds_dwordx4 v254, s[66:67]
	s_add_u32 s3, s28, s52
	s_addc_u32 s7, s29, s53
	s_lshl_b32 s35, s33, 19
	s_and_b32 s35, s35, 0x300000
	s_add_u32 s50, s3, s35
	s_addc_u32 s51, s7, 0
	s_ashr_i32 s43, s42, 31
	s_lshl_b32 s7, s58, 8
	s_lshl_b64 s[54:55], s[42:43], 21
	v_lshlrev_b32_e32 v162, 4, v0
	v_and_b32_e32 v2, 32, v0
	s_add_u32 s35, s30, s54
	v_bitop3_b32 v12, v162, v2, 48 bitop3:0x6c
	v_and_b32_e32 v13, 64, v0
	s_addc_u32 s38, s31, s55
	s_lshl_b32 s3, s58, 20
	v_lshrrev_b32_e32 v4, 3, v0
	v_bfe_u32 v3, v0, 2, 4
	v_or_b32_e32 v2, v12, v13
	v_or_b32_e32 v164, 0x2000, v162
	s_add_u32 s56, s35, s3
	v_and_or_b32 v4, v4, 48, v3
	v_lshrrev_b32_e32 v2, 1, v2
	v_lshrrev_b32_e32 v5, 7, v164
	s_movk_i32 s35, 0x70
	v_add_u32_e32 v142, 0, v162
	v_lshl_or_b32 v4, v4, 11, v2
	v_and_or_b32 v5, v5, s35, v3
	v_readfirstlane_b32 s35, v142
	v_add_u32_e32 v143, 0x2000, v142
	v_lshlrev_b32_e32 v130, 1, v4
	s_mov_b32 m0, s35
	v_readfirstlane_b32 s35, v143
	s_addc_u32 s57, s38, 0
	s_add_u32 s84, s56, s81
	s_addc_u32 s85, s57, 0
	s_add_u32 s86, s84, 0x80000
	s_addc_u32 s87, s85, 0
	s_mov_b32 m0, s35
	s_add_i32 s35, 0, 0x10000
	v_lshl_or_b32 v2, v5, 11, v2
	v_add_u32_e32 v144, s35, v162
	v_lshlrev_b32_e32 v132, 1, v2
	v_readfirstlane_b32 s38, v144
	v_add_u32_e32 v145, 0x2000, v144
	s_mov_b32 m0, s38
	v_readfirstlane_b32 s38, v145
	v_add_u32_e32 v151, 0x4000, v142
	global_load_lds_dwordx4 v130, s[84:85]
	s_mov_b32 m0, s38
	s_add_u32 s38, s50, 0x80000
	v_readfirstlane_b32 s44, v151
	v_add_u32_e32 v153, 0x6000, v142
	global_load_lds_dwordx4 v132, s[84:85]
	s_addc_u32 s39, s51, 0
	s_mov_b32 m0, s44
	v_readfirstlane_b32 s44, v153
	s_mov_b32 m0, s44
	v_mov_b32_e32 v2, 0
	s_add_u32 s38, s56, 0x80000
	s_addc_u32 s39, s57, 0
	s_add_i32 s60, 0, 0x14000
	v_add_u32_e32 v154, s60, v162
	v_add_u32_e32 v155, 0x2000, v154
	v_readfirstlane_b32 s44, v154
	s_mov_b32 m0, s44
	v_readfirstlane_b32 s44, v155
	global_load_lds_dwordx4 v130, s[86:87]
	s_mov_b32 m0, s44
	v_lshrrev_b32_e32 v14, 8, v0
	global_load_lds_dwordx4 v132, s[86:87]
	v_mov_b32_e32 v131, v2
	v_mov_b32_e32 v133, v2
	v_lshl_add_u64 v[10:11], s[50:51], 0, v[130:131]
	v_lshl_add_u64 v[8:9], s[50:51], 0, v[132:133]
	v_lshl_add_u64 v[6:7], s[56:57], 0, v[130:131]
	v_lshl_add_u64 v[4:5], s[56:57], 0, v[132:133]
	v_cmp_eq_u32_e32 vcc, 1, v14
	s_and_saveexec_b64 s[38:39], vcc
	s_cbranch_execz .LBB5_8
	s_barrier
.LBB5_8:
	s_or_b64 exec, exec, s[38:39]
	v_add_u32_e32 v156, 0x8000, v142
	s_load_dwordx2 s[38:39], s[0:1], 0x78
	s_load_dwordx2 s[44:45], s[0:1], 0x68
	s_load_dwordx2 s[48:49], s[0:1], 0x28
	s_mov_b64 s[0:1], 0x80
	s_mov_b32 s0, s83
	v_readfirstlane_b32 s61, v156
	v_add_u32_e32 v157, 0xa000, v142
	v_lshl_add_u64 v[10:11], v[10:11], 0, s[0:1]
	s_mov_b32 m0, s61
	v_readfirstlane_b32 s61, v157
	s_waitcnt vmcnt(2)
	s_barrier
	global_load_lds_dwordx4 v[10:11], off
	s_mov_b32 m0, s61
	s_add_i32 s61, 0, 0x18000
	v_add_u32_e32 v158, s61, v162
	v_lshl_add_u64 v[8:9], v[8:9], 0, s[0:1]
	v_readfirstlane_b32 s62, v158
	s_add_u32 s56, s56, s82
	global_load_lds_dwordx4 v[8:9], off
	s_mov_b32 m0, s62
	v_add_u32_e32 v159, 0x2000, v158
	s_addc_u32 s57, s57, 0
	s_add_i32 s62, 0, 0x1c000
	v_lshl_add_u64 v[6:7], v[6:7], 0, s[0:1]
	v_lshl_add_u64 v[4:5], v[4:5], 0, s[0:1]
	v_readfirstlane_b32 s0, v159
	v_add_u32_e32 v160, s62, v162
	global_load_lds_dwordx4 v[6:7], off
	s_mov_b32 m0, s0
	v_readfirstlane_b32 s63, v160
	v_add_u32_e32 v161, 0x2000, v160
	global_load_lds_dwordx4 v[4:5], off
	s_mov_b32 m0, s63
	v_readfirstlane_b32 s63, v161
	global_load_lds_dwordx4 v130, s[56:57]
	s_mov_b32 m0, s63
	v_lshlrev_b32_e32 v4, 6, v0
	global_load_lds_dwordx4 v132, s[56:57]
	v_lshlrev_b32_e32 v185, 2, v0
	v_and_b32_e32 v146, 48, v0
	v_and_b32_e32 v5, 0x3c0, v4
	v_and_b32_e32 v152, 32, v185
	v_bitop3_b32 v5, v5, v152, v146 bitop3:0x36
	s_add_u32 s3, s54, s3
	v_add_u32_e32 v8, s35, v5
	s_addc_u32 s35, s55, 0
	s_add_u32 s30, s30, s3
	s_addc_u32 s31, s31, s35
	s_lshl_b32 s2, s2, 16
	v_and_b32_e32 v15, 0x3000, v4
	v_add_u16_e32 v4, v12, v13
	s_and_b32 s2, s2, 0x300000
	v_lshrrev_b16_e32 v6, 1, v4
	v_lshlrev_b32_e32 v4, 8, v0
	v_lshlrev_b32_e32 v7, 4, v164
	s_add_u32 s2, s52, s2
	v_and_b32_e32 v4, 0x18000, v4
	v_lshlrev_b32_e32 v3, 11, v3
	v_and_b32_e32 v7, 0x38000, v7
	s_addc_u32 s3, s53, 0
	s_waitcnt vmcnt(6)
	v_lshlrev_b32_e32 v14, 13, v14
	v_or3_b32 v4, v6, v4, v3
	v_or3_b32 v3, v6, v7, v3
	s_add_u32 s2, s28, s2
	v_add_u32_e32 v9, s60, v5
	v_add_u32_e32 v10, s61, v5
	v_add_u32_e32 v11, s62, v5
	v_add_u32_e32 v16, 0, v5
	v_or_b32_e32 v17, 0x800, v14
	v_or_b32_e32 v18, 0x1000, v14
	v_or_b32_e32 v19, 0x1800, v14
	v_lshlrev_b32_e32 v4, 1, v4
	v_mov_b32_e32 v5, v2
	v_lshlrev_b32_e32 v6, 1, v3
	v_mov_b32_e32 v7, v2
	s_addc_u32 s3, s29, s3
	s_mov_b64 s[0:1], 0x80080
	v_lshl_add_u64 v[134:135], s[30:31], 0, v[4:5]
	v_lshl_add_u64 v[136:137], s[30:31], 0, v[6:7]
	v_lshl_add_u64 v[138:139], s[2:3], 0, v[4:5]
	v_lshl_add_u64 v[140:141], s[2:3], 0, v[6:7]
	s_mov_b32 s35, -2
	s_mov_b64 s[2:3], 0
	v_add_u32_e32 v165, v8, v15
	v_add_u32_e32 v150, v16, v14
	v_add_u32_e32 v149, v16, v17
	v_add_u32_e32 v148, v16, v18
	v_add_u32_e32 v147, v16, v19
	v_add_u32_e32 v163, v9, v15
	s_mov_b64 s[28:29], 0x100
	s_mov_b64 s[30:31], 0x80100
	v_add_u32_e32 v133, v10, v15
	s_mov_b64 s[52:53], 0x180
	s_mov_b64 s[54:55], 0x80180
	s_mov_b32 s0, s82
	s_add_u32 s28, s81, 0x100
	s_and_b32 s28, s28, 0xfff
	s_or_b32 s30, s28, 0x80000
	s_add_u32 s52, s81, 0x180
	s_and_b32 s52, s52, 0xfff
	s_or_b32 s54, s52, 0x80000
	s_mov_b32 s80, 0
	v_add_u32_e32 v131, v11, v15
	v_mov_b32_e32 v3, v2
	v_mov_b32_e32 v4, v2
	v_mov_b32_e32 v6, v2
	v_mov_b32_e32 v8, v2
	v_mov_b32_e32 v9, v2
	v_mov_b32_e32 v10, v2
	v_mov_b32_e32 v11, v2
	v_mov_b32_e32 v12, v2
	v_mov_b32_e32 v13, v2
	v_mov_b32_e32 v14, v2
	v_mov_b32_e32 v15, v2
	v_mov_b32_e32 v16, v2
	v_mov_b32_e32 v17, v2
	v_mov_b32_e32 v18, v2
	v_mov_b32_e32 v19, v2
	v_mov_b32_e32 v20, v2
	v_mov_b32_e32 v21, v2
	v_mov_b32_e32 v22, v2
	v_mov_b32_e32 v23, v2
	v_mov_b32_e32 v24, v2
	v_mov_b32_e32 v25, v2
	v_mov_b32_e32 v26, v2
	v_mov_b32_e32 v27, v2
	v_mov_b32_e32 v28, v2
	v_mov_b32_e32 v29, v2
	v_mov_b32_e32 v30, v2
	v_mov_b32_e32 v31, v2
	v_mov_b32_e32 v32, v2
	v_mov_b32_e32 v33, v2
	v_mov_b32_e32 v34, v2
	v_mov_b32_e32 v35, v2
	v_mov_b32_e32 v36, v2
	v_mov_b32_e32 v37, v2
	v_mov_b32_e32 v38, v2
	v_mov_b32_e32 v39, v2
	v_mov_b32_e32 v40, v2
	v_mov_b32_e32 v41, v2
	v_mov_b32_e32 v42, v2
	v_mov_b32_e32 v43, v2
	v_mov_b32_e32 v44, v2
	v_mov_b32_e32 v45, v2
	v_mov_b32_e32 v46, v2
	v_mov_b32_e32 v47, v2
	v_mov_b32_e32 v48, v2
	v_mov_b32_e32 v49, v2
	v_mov_b32_e32 v50, v2
	v_mov_b32_e32 v51, v2
	v_mov_b32_e32 v52, v2
	v_mov_b32_e32 v53, v2
	v_mov_b32_e32 v54, v2
	v_mov_b32_e32 v55, v2
	v_mov_b32_e32 v56, v2
	v_mov_b32_e32 v57, v2
	v_mov_b32_e32 v58, v2
	v_mov_b32_e32 v59, v2
	v_mov_b32_e32 v60, v2
	v_mov_b32_e32 v61, v2
	v_mov_b32_e32 v62, v2
	v_mov_b32_e32 v63, v2
	v_mov_b32_e32 v64, v2
	v_mov_b32_e32 v65, v2
	v_mov_b32_e32 v66, v2
	v_mov_b32_e32 v67, v2
	v_mov_b32_e32 v68, v2
	v_mov_b32_e32 v69, v2
	v_mov_b32_e32 v70, v2
	v_mov_b32_e32 v71, v2
	v_mov_b32_e32 v72, v2
	v_mov_b32_e32 v73, v2
	v_mov_b32_e32 v74, v2
	v_mov_b32_e32 v75, v2
	v_mov_b32_e32 v76, v2
	v_mov_b32_e32 v77, v2
	v_mov_b32_e32 v78, v2
	v_mov_b32_e32 v79, v2
	v_mov_b32_e32 v80, v2
	v_mov_b32_e32 v81, v2
	v_mov_b32_e32 v82, v2
	v_mov_b32_e32 v83, v2
	v_mov_b32_e32 v84, v2
	v_mov_b32_e32 v85, v2
	v_mov_b32_e32 v86, v2
	v_mov_b32_e32 v87, v2
	v_mov_b32_e32 v88, v2
	v_mov_b32_e32 v89, v2
	v_mov_b32_e32 v90, v2
	v_mov_b32_e32 v91, v2
	v_mov_b32_e32 v92, v2
	v_mov_b32_e32 v93, v2
	v_mov_b32_e32 v94, v2
	v_mov_b32_e32 v95, v2
	v_mov_b32_e32 v96, v2
	v_mov_b32_e32 v97, v2
	v_mov_b32_e32 v98, v2
	v_mov_b32_e32 v99, v2
	v_mov_b32_e32 v100, v2
	v_mov_b32_e32 v101, v2
	v_mov_b32_e32 v102, v2
	v_mov_b32_e32 v103, v2
	v_mov_b32_e32 v104, v2
	v_mov_b32_e32 v105, v2
	v_mov_b32_e32 v106, v2
	v_mov_b32_e32 v107, v2
	v_mov_b32_e32 v108, v2
	v_mov_b32_e32 v109, v2
	v_mov_b32_e32 v110, v2
	v_mov_b32_e32 v111, v2
	v_mov_b32_e32 v112, v2
	v_mov_b32_e32 v113, v2
	v_mov_b32_e32 v114, v2
	v_mov_b32_e32 v115, v2
	v_mov_b32_e32 v116, v2
	v_mov_b32_e32 v117, v2
	v_mov_b32_e32 v118, v2
	v_mov_b32_e32 v119, v2
	v_mov_b32_e32 v120, v2
	v_mov_b32_e32 v121, v2
	v_mov_b32_e32 v122, v2
	v_mov_b32_e32 v123, v2
	v_mov_b32_e32 v124, v2
	v_mov_b32_e32 v125, v2
	v_mov_b32_e32 v126, v2
	v_mov_b32_e32 v127, v2
	v_mov_b32_e32 v128, v2
	v_mov_b32_e32 v129, v2
	v_lshrrev_b32_e32 v190, 2, v0
	v_and_b32_e32 v186, 48, v162
	v_and_b32_e32 v188, 15, v0
	v_add_u32_e32 v166, 0xc000, v142
	v_add_u32_e32 v167, 0xe000, v142
	s_barrier
.LBB5_9:
	ds_read_b128 v[168:171], v165
	ds_read_b128 v[172:175], v165 offset:1024
	ds_read_b128 v[176:179], v165 offset:2048
	ds_read_b128 v[192:195], v165 offset:3072
	v_lshl_add_u64 v[244:245], v[138:139], 0, s[2:3]
	v_readfirstlane_b32 s56, v166
	v_lshl_add_u64 v[196:197], v[244:245], 0, s[0:1]
	s_mov_b32 m0, s56
	v_lshl_add_u64 v[246:247], v[140:141], 0, s[2:3]
	v_readfirstlane_b32 s56, v167
	global_load_lds_dwordx4 v[196:197], off
	v_lshl_add_u64 v[196:197], v[246:247], 0, s[0:1]
	s_mov_b32 m0, s56
	s_nop 0
	global_load_lds_dwordx4 v[196:197], off
	ds_read_b128 v[196:199], v150
	ds_read_b128 v[200:203], v150 offset:1024
	ds_read_b128 v[204:207], v149
	ds_read_b128 v[208:211], v149 offset:1024
	ds_read_b128 v[212:215], v148
	ds_read_b128 v[216:219], v148 offset:1024
	ds_read_b128 v[220:223], v147
	ds_read_b128 v[224:227], v147 offset:1024
	s_waitcnt lgkmcnt(8)
	s_barrier
	s_waitcnt lgkmcnt(0)
	s_setprio 1
	s_waitcnt lgkmcnt(0)
	v_mfma_f32_16x16x32_f16 v[126:129], v[168:171], v[196:199], v[126:129]
	v_mfma_f32_16x16x32_f16 v[122:125], v[176:179], v[196:199], v[122:125]
	v_mfma_f32_16x16x32_f16 v[118:121], v[168:171], v[204:207], v[118:121]
	v_mfma_f32_16x16x32_f16 v[114:117], v[176:179], v[204:207], v[114:117]
	v_mfma_f32_16x16x32_f16 v[110:113], v[168:171], v[212:215], v[110:113]
	v_mfma_f32_16x16x32_f16 v[106:109], v[176:179], v[212:215], v[106:109]
	v_mfma_f32_16x16x32_f16 v[102:105], v[168:171], v[220:223], v[102:105]
	v_mfma_f32_16x16x32_f16 v[98:101], v[176:179], v[220:223], v[98:101]
	v_mfma_f32_16x16x32_f16 v[126:129], v[172:175], v[200:203], v[126:129]
	v_mfma_f32_16x16x32_f16 v[122:125], v[192:195], v[200:203], v[122:125]
	v_mfma_f32_16x16x32_f16 v[118:121], v[172:175], v[208:211], v[118:121]
	v_mfma_f32_16x16x32_f16 v[114:117], v[192:195], v[208:211], v[114:117]
	v_mfma_f32_16x16x32_f16 v[110:113], v[172:175], v[216:219], v[110:113]
	v_mfma_f32_16x16x32_f16 v[106:109], v[192:195], v[216:219], v[106:109]
	v_mfma_f32_16x16x32_f16 v[102:105], v[172:175], v[224:227], v[102:105]
	v_mfma_f32_16x16x32_f16 v[98:101], v[192:195], v[224:227], v[98:101]
	s_setprio 0
	s_barrier
	v_lshl_add_u64 v[248:249], v[134:135], 0, s[2:3]
	v_readfirstlane_b32 s56, v144
	v_lshl_add_u64 v[250:251], v[248:249], 0, s[28:29]
	s_mov_b32 m0, s56
	ds_read_b128 v[228:231], v163
	ds_read_b128 v[232:235], v163 offset:1024
	ds_read_b128 v[236:239], v163 offset:2048
	ds_read_b128 v[240:243], v163 offset:3072
	global_load_lds_dwordx4 v[250:251], off
	v_lshl_add_u64 v[250:251], v[136:137], 0, s[2:3]
	v_readfirstlane_b32 s56, v145
	v_lshl_add_u64 v[252:253], v[250:251], 0, s[28:29]
	s_mov_b32 m0, s56
	s_nop 0
	global_load_lds_dwordx4 v[252:253], off
	s_barrier
	s_waitcnt lgkmcnt(0)
	s_setprio 1
	s_waitcnt lgkmcnt(0)
	v_mfma_f32_16x16x32_f16 v[94:97], v[228:231], v[196:199], v[94:97]
	v_mfma_f32_16x16x32_f16 v[90:93], v[236:239], v[196:199], v[90:93]
	v_mfma_f32_16x16x32_f16 v[86:89], v[228:231], v[204:207], v[86:89]
	v_mfma_f32_16x16x32_f16 v[82:85], v[236:239], v[204:207], v[82:85]
	v_mfma_f32_16x16x32_f16 v[78:81], v[228:231], v[212:215], v[78:81]
	v_mfma_f32_16x16x32_f16 v[74:77], v[236:239], v[212:215], v[74:77]
	v_mfma_f32_16x16x32_f16 v[70:73], v[228:231], v[220:223], v[70:73]
	v_mfma_f32_16x16x32_f16 v[66:69], v[236:239], v[220:223], v[66:69]
	v_mfma_f32_16x16x32_f16 v[94:97], v[232:235], v[200:203], v[94:97]
	v_mfma_f32_16x16x32_f16 v[90:93], v[240:243], v[200:203], v[90:93]
	v_mfma_f32_16x16x32_f16 v[86:89], v[232:235], v[208:211], v[86:89]
	v_mfma_f32_16x16x32_f16 v[82:85], v[240:243], v[208:211], v[82:85]
	v_mfma_f32_16x16x32_f16 v[78:81], v[232:235], v[216:219], v[78:81]
	v_mfma_f32_16x16x32_f16 v[74:77], v[240:243], v[216:219], v[74:77]
	v_mfma_f32_16x16x32_f16 v[70:73], v[232:235], v[224:227], v[70:73]
	v_mfma_f32_16x16x32_f16 v[66:69], v[240:243], v[224:227], v[66:69]
	s_setprio 0
	v_readfirstlane_b32 s56, v142
	v_lshl_add_u64 v[252:253], v[244:245], 0, s[28:29]
	s_mov_b32 m0, s56
	v_readfirstlane_b32 s56, v143
	s_barrier
	ds_read_b128 v[196:199], v150 offset:16384
	ds_read_b128 v[200:203], v150 offset:17408
	ds_read_b128 v[204:207], v149 offset:16384
	ds_read_b128 v[208:211], v149 offset:17408
	ds_read_b128 v[212:215], v148 offset:16384
	ds_read_b128 v[216:219], v148 offset:17408
	ds_read_b128 v[220:223], v147 offset:16384
	ds_read_b128 v[224:227], v147 offset:17408
	global_load_lds_dwordx4 v[252:253], off
	v_lshl_add_u64 v[252:253], v[246:247], 0, s[28:29]
	s_mov_b32 m0, s56
	s_nop 0
	global_load_lds_dwordx4 v[252:253], off
	s_barrier
	s_waitcnt lgkmcnt(0)
	s_setprio 1
	s_waitcnt lgkmcnt(0)
	v_mfma_f32_16x16x32_f16 v[62:65], v[168:171], v[196:199], v[62:65]
	v_mfma_f32_16x16x32_f16 v[58:61], v[176:179], v[196:199], v[58:61]
	v_mfma_f32_16x16x32_f16 v[54:57], v[168:171], v[204:207], v[54:57]
	v_mfma_f32_16x16x32_f16 v[50:53], v[176:179], v[204:207], v[50:53]
	v_mfma_f32_16x16x32_f16 v[46:49], v[168:171], v[212:215], v[46:49]
	v_mfma_f32_16x16x32_f16 v[42:45], v[176:179], v[212:215], v[42:45]
	v_mfma_f32_16x16x32_f16 v[38:41], v[168:171], v[220:223], v[38:41]
	v_mfma_f32_16x16x32_f16 v[34:37], v[176:179], v[220:223], v[34:37]
	v_mfma_f32_16x16x32_f16 v[62:65], v[172:175], v[200:203], v[62:65]
	v_mfma_f32_16x16x32_f16 v[58:61], v[192:195], v[200:203], v[58:61]
	v_mfma_f32_16x16x32_f16 v[54:57], v[172:175], v[208:211], v[54:57]
	v_mfma_f32_16x16x32_f16 v[50:53], v[192:195], v[208:211], v[50:53]
	v_mfma_f32_16x16x32_f16 v[46:49], v[172:175], v[216:219], v[46:49]
	v_mfma_f32_16x16x32_f16 v[42:45], v[192:195], v[216:219], v[42:45]
	v_mfma_f32_16x16x32_f16 v[38:41], v[172:175], v[224:227], v[38:41]
	v_mfma_f32_16x16x32_f16 v[34:37], v[192:195], v[224:227], v[34:37]
	s_setprio 0
	s_barrier
	v_readfirstlane_b32 s56, v154
	v_lshl_add_u64 v[168:169], v[248:249], 0, s[30:31]
	s_mov_b32 m0, s56
	v_readfirstlane_b32 s56, v155
	global_load_lds_dwordx4 v[168:169], off
	v_lshl_add_u64 v[168:169], v[250:251], 0, s[30:31]
	s_mov_b32 m0, s56
	s_nop 0
	global_load_lds_dwordx4 v[168:169], off
	s_waitcnt vmcnt(6)
	s_barrier
	s_setprio 1
	v_mfma_f32_16x16x32_f16 v[30:33], v[228:231], v[196:199], v[30:33]
	v_mfma_f32_16x16x32_f16 v[26:29], v[236:239], v[196:199], v[26:29]
	v_mfma_f32_16x16x32_f16 v[22:25], v[228:231], v[204:207], v[22:25]
	v_mfma_f32_16x16x32_f16 v[18:21], v[236:239], v[204:207], v[18:21]
	v_mfma_f32_16x16x32_f16 v[14:17], v[228:231], v[212:215], v[14:17]
	v_mfma_f32_16x16x32_f16 v[10:13], v[236:239], v[212:215], v[10:13]
	v_mfma_f32_16x16x32_f16 v[6:9], v[228:231], v[220:223], v[6:9]
	v_mfma_f32_16x16x32_f16 v[2:5], v[236:239], v[220:223], v[2:5]
	v_mfma_f32_16x16x32_f16 v[30:33], v[232:235], v[200:203], v[30:33]
	v_mfma_f32_16x16x32_f16 v[26:29], v[240:243], v[200:203], v[26:29]
	v_mfma_f32_16x16x32_f16 v[22:25], v[232:235], v[208:211], v[22:25]
	v_mfma_f32_16x16x32_f16 v[18:21], v[240:243], v[208:211], v[18:21]
	v_mfma_f32_16x16x32_f16 v[14:17], v[232:235], v[216:219], v[14:17]
	v_mfma_f32_16x16x32_f16 v[10:13], v[240:243], v[216:219], v[10:13]
	v_mfma_f32_16x16x32_f16 v[6:9], v[232:235], v[224:227], v[6:9]
	v_mfma_f32_16x16x32_f16 v[2:5], v[240:243], v[224:227], v[2:5]
	s_setprio 0
	s_barrier
	ds_read_b128 v[168:171], v133
	ds_read_b128 v[172:175], v133 offset:1024
	ds_read_b128 v[176:179], v133 offset:2048
	ds_read_b128 v[192:195], v133 offset:3072
	v_readfirstlane_b32 s56, v151
	v_lshl_add_u64 v[228:229], v[244:245], 0, s[30:31]
	s_mov_b32 m0, s56
	v_readfirstlane_b32 s56, v153
	ds_read_b128 v[196:199], v150 offset:32768
	ds_read_b128 v[200:203], v150 offset:33792
	ds_read_b128 v[204:207], v149 offset:32768
	ds_read_b128 v[208:211], v149 offset:33792
	ds_read_b128 v[212:215], v148 offset:32768
	ds_read_b128 v[216:219], v148 offset:33792
	ds_read_b128 v[220:223], v147 offset:32768
	ds_read_b128 v[224:227], v147 offset:33792
	global_load_lds_dwordx4 v[228:229], off
	v_lshl_add_u64 v[228:229], v[246:247], 0, s[30:31]
	s_mov_b32 m0, s56
	s_nop 0
	global_load_lds_dwordx4 v[228:229], off
	s_waitcnt lgkmcnt(8)
	s_barrier
	s_waitcnt lgkmcnt(0)
	s_setprio 1
	s_waitcnt lgkmcnt(0)
	v_mfma_f32_16x16x32_f16 v[126:129], v[168:171], v[196:199], v[126:129]
	v_mfma_f32_16x16x32_f16 v[122:125], v[176:179], v[196:199], v[122:125]
	v_mfma_f32_16x16x32_f16 v[118:121], v[168:171], v[204:207], v[118:121]
	v_mfma_f32_16x16x32_f16 v[114:117], v[176:179], v[204:207], v[114:117]
	v_mfma_f32_16x16x32_f16 v[110:113], v[168:171], v[212:215], v[110:113]
	v_mfma_f32_16x16x32_f16 v[106:109], v[176:179], v[212:215], v[106:109]
	v_mfma_f32_16x16x32_f16 v[102:105], v[168:171], v[220:223], v[102:105]
	v_mfma_f32_16x16x32_f16 v[98:101], v[176:179], v[220:223], v[98:101]
	v_mfma_f32_16x16x32_f16 v[126:129], v[172:175], v[200:203], v[126:129]
	v_mfma_f32_16x16x32_f16 v[122:125], v[192:195], v[200:203], v[122:125]
	v_mfma_f32_16x16x32_f16 v[118:121], v[172:175], v[208:211], v[118:121]
	v_mfma_f32_16x16x32_f16 v[114:117], v[192:195], v[208:211], v[114:117]
	v_mfma_f32_16x16x32_f16 v[110:113], v[172:175], v[216:219], v[110:113]
	v_mfma_f32_16x16x32_f16 v[106:109], v[192:195], v[216:219], v[106:109]
	v_mfma_f32_16x16x32_f16 v[102:105], v[172:175], v[224:227], v[102:105]
	v_mfma_f32_16x16x32_f16 v[98:101], v[192:195], v[224:227], v[98:101]
	s_setprio 0
	s_barrier
	v_readfirstlane_b32 s56, v158
	v_lshl_add_u64 v[252:253], v[248:249], 0, s[52:53]
	s_mov_b32 m0, s56
	v_readfirstlane_b32 s56, v159
	ds_read_b128 v[228:231], v131
	ds_read_b128 v[232:235], v131 offset:1024
	ds_read_b128 v[236:239], v131 offset:2048
	ds_read_b128 v[240:243], v131 offset:3072
	global_load_lds_dwordx4 v[252:253], off
	v_lshl_add_u64 v[252:253], v[250:251], 0, s[52:53]
	s_mov_b32 m0, s56
	s_nop 0
	global_load_lds_dwordx4 v[252:253], off
	s_barrier
	s_waitcnt lgkmcnt(0)
	s_setprio 1
	s_waitcnt lgkmcnt(0)
	v_mfma_f32_16x16x32_f16 v[94:97], v[228:231], v[196:199], v[94:97]
	v_mfma_f32_16x16x32_f16 v[90:93], v[236:239], v[196:199], v[90:93]
	v_mfma_f32_16x16x32_f16 v[86:89], v[228:231], v[204:207], v[86:89]
	v_mfma_f32_16x16x32_f16 v[82:85], v[236:239], v[204:207], v[82:85]
	v_mfma_f32_16x16x32_f16 v[78:81], v[228:231], v[212:215], v[78:81]
	v_mfma_f32_16x16x32_f16 v[74:77], v[236:239], v[212:215], v[74:77]
	v_mfma_f32_16x16x32_f16 v[70:73], v[228:231], v[220:223], v[70:73]
	v_mfma_f32_16x16x32_f16 v[66:69], v[236:239], v[220:223], v[66:69]
	v_mfma_f32_16x16x32_f16 v[94:97], v[232:235], v[200:203], v[94:97]
	v_mfma_f32_16x16x32_f16 v[90:93], v[240:243], v[200:203], v[90:93]
	v_mfma_f32_16x16x32_f16 v[86:89], v[232:235], v[208:211], v[86:89]
	v_mfma_f32_16x16x32_f16 v[82:85], v[240:243], v[208:211], v[82:85]
	v_mfma_f32_16x16x32_f16 v[78:81], v[232:235], v[216:219], v[78:81]
	v_mfma_f32_16x16x32_f16 v[74:77], v[240:243], v[216:219], v[74:77]
	v_mfma_f32_16x16x32_f16 v[70:73], v[232:235], v[224:227], v[70:73]
	v_mfma_f32_16x16x32_f16 v[66:69], v[240:243], v[224:227], v[66:69]
	s_setprio 0
	v_readfirstlane_b32 s56, v156
	v_lshl_add_u64 v[244:245], v[244:245], 0, s[52:53]
	s_mov_b32 m0, s56
	v_readfirstlane_b32 s56, v157
	s_barrier
	ds_read_b128 v[196:199], v150 offset:49152
	ds_read_b128 v[200:203], v150 offset:50176
	ds_read_b128 v[204:207], v149 offset:49152
	ds_read_b128 v[208:211], v149 offset:50176
	ds_read_b128 v[212:215], v148 offset:49152
	ds_read_b128 v[216:219], v148 offset:50176
	ds_read_b128 v[220:223], v147 offset:49152
	ds_read_b128 v[224:227], v147 offset:50176
	global_load_lds_dwordx4 v[244:245], off
	v_lshl_add_u64 v[244:245], v[246:247], 0, s[52:53]
	s_mov_b32 m0, s56
	s_nop 0
	global_load_lds_dwordx4 v[244:245], off
	s_barrier
	s_waitcnt lgkmcnt(0)
	s_setprio 1
	s_waitcnt lgkmcnt(0)
	v_mfma_f32_16x16x32_f16 v[62:65], v[168:171], v[196:199], v[62:65]
	v_mfma_f32_16x16x32_f16 v[58:61], v[176:179], v[196:199], v[58:61]
	v_mfma_f32_16x16x32_f16 v[54:57], v[168:171], v[204:207], v[54:57]
	v_mfma_f32_16x16x32_f16 v[50:53], v[176:179], v[204:207], v[50:53]
	v_mfma_f32_16x16x32_f16 v[46:49], v[168:171], v[212:215], v[46:49]
	v_mfma_f32_16x16x32_f16 v[42:45], v[176:179], v[212:215], v[42:45]
	v_mfma_f32_16x16x32_f16 v[38:41], v[168:171], v[220:223], v[38:41]
	v_mfma_f32_16x16x32_f16 v[34:37], v[176:179], v[220:223], v[34:37]
	v_mfma_f32_16x16x32_f16 v[62:65], v[172:175], v[200:203], v[62:65]
	v_mfma_f32_16x16x32_f16 v[58:61], v[192:195], v[200:203], v[58:61]
	v_mfma_f32_16x16x32_f16 v[54:57], v[172:175], v[208:211], v[54:57]
	v_mfma_f32_16x16x32_f16 v[50:53], v[192:195], v[208:211], v[50:53]
	v_mfma_f32_16x16x32_f16 v[46:49], v[172:175], v[216:219], v[46:49]
	v_mfma_f32_16x16x32_f16 v[42:45], v[192:195], v[216:219], v[42:45]
	v_mfma_f32_16x16x32_f16 v[38:41], v[172:175], v[224:227], v[38:41]
	v_mfma_f32_16x16x32_f16 v[34:37], v[192:195], v[224:227], v[34:37]
	s_setprio 0
	s_barrier
	v_readfirstlane_b32 s56, v160
	v_lshl_add_u64 v[168:169], v[248:249], 0, s[54:55]
	s_mov_b32 m0, s56
	v_readfirstlane_b32 s56, v161
	global_load_lds_dwordx4 v[168:169], off
	v_lshl_add_u64 v[168:169], v[250:251], 0, s[54:55]
	s_mov_b32 m0, s56
	s_nop 0
	global_load_lds_dwordx4 v[168:169], off
	s_waitcnt vmcnt(6)
	s_barrier
	s_setprio 1
	v_mfma_f32_16x16x32_f16 v[30:33], v[228:231], v[196:199], v[30:33]
	v_mfma_f32_16x16x32_f16 v[26:29], v[236:239], v[196:199], v[26:29]
	v_mfma_f32_16x16x32_f16 v[22:25], v[228:231], v[204:207], v[22:25]
	v_mfma_f32_16x16x32_f16 v[18:21], v[236:239], v[204:207], v[18:21]
	v_mfma_f32_16x16x32_f16 v[14:17], v[228:231], v[212:215], v[14:17]
	v_mfma_f32_16x16x32_f16 v[10:13], v[236:239], v[212:215], v[10:13]
	v_mfma_f32_16x16x32_f16 v[6:9], v[228:231], v[220:223], v[6:9]
	v_mfma_f32_16x16x32_f16 v[2:5], v[236:239], v[220:223], v[2:5]
	v_mfma_f32_16x16x32_f16 v[30:33], v[232:235], v[200:203], v[30:33]
	v_mfma_f32_16x16x32_f16 v[26:29], v[240:243], v[200:203], v[26:29]
	v_mfma_f32_16x16x32_f16 v[22:25], v[232:235], v[208:211], v[22:25]
	v_mfma_f32_16x16x32_f16 v[18:21], v[240:243], v[208:211], v[18:21]
	v_mfma_f32_16x16x32_f16 v[14:17], v[232:235], v[216:219], v[14:17]
	v_mfma_f32_16x16x32_f16 v[10:13], v[240:243], v[216:219], v[10:13]
	v_mfma_f32_16x16x32_f16 v[6:9], v[232:235], v[224:227], v[6:9]
	v_mfma_f32_16x16x32_f16 v[2:5], v[240:243], v[224:227], v[2:5]
	s_setprio 0
	s_add_i32 s35, s35, 2
	s_add_u32 s80, s80, 0x100
	s_add_u32 s89, s80, s81
	s_add_u32 s0, s89, 0x80
	s_and_b32 s0, s0, 0xfff
	s_or_b32 s0, s0, 0x80000
	s_add_u32 s28, s89, 0x100
	s_and_b32 s28, s28, 0xfff
	s_or_b32 s30, s28, 0x80000
	s_add_u32 s52, s89, 0x180
	s_and_b32 s52, s52, 0xfff
	s_or_b32 s54, s52, 0x80000
	s_cmp_lt_u32 s35, 28
	s_barrier
	s_cbranch_scc1 .LBB5_9
	v_add_u32_e32 v143, 0xc000, v142
	s_add_u32 s0, s50, s88
	v_readfirstlane_b32 s2, v143
	s_addc_u32 s1, s51, 0
	s_mov_b32 m0, s2
	ds_read_b128 v[134:137], v165
	ds_read_b128 v[138:141], v165 offset:1024
	ds_read_b128 v[154:157], v165 offset:2048
	ds_read_b128 v[158:161], v165 offset:3072
	global_load_lds_dwordx4 v130, s[0:1]
	v_add_u32_e32 v130, 0xe000, v142
	s_nop 0
	v_readfirstlane_b32 s2, v130
	s_mov_b32 m0, s2
	s_nop 0
	global_load_lds_dwordx4 v132, s[0:1]
	ds_read_b128 v[142:145], v150
	ds_read_b128 v[166:169], v150 offset:1024
	ds_read_b128 v[170:173], v149
	ds_read_b128 v[174:177], v149 offset:1024
	ds_read_b128 v[192:195], v148
	ds_read_b128 v[196:199], v148 offset:1024
	ds_read_b128 v[200:203], v147
	ds_read_b128 v[204:207], v147 offset:1024
	s_barrier
	s_waitcnt lgkmcnt(0)
	s_setprio 1
	s_waitcnt lgkmcnt(0)
	v_mfma_f32_16x16x32_f16 v[126:129], v[134:137], v[142:145], v[126:129]
	v_mfma_f32_16x16x32_f16 v[122:125], v[154:157], v[142:145], v[122:125]
	v_mfma_f32_16x16x32_f16 v[118:121], v[134:137], v[170:173], v[118:121]
	v_mfma_f32_16x16x32_f16 v[114:117], v[154:157], v[170:173], v[114:117]
	v_mfma_f32_16x16x32_f16 v[110:113], v[134:137], v[192:195], v[110:113]
	v_mfma_f32_16x16x32_f16 v[106:109], v[154:157], v[192:195], v[106:109]
	v_mfma_f32_16x16x32_f16 v[102:105], v[134:137], v[200:203], v[102:105]
	v_mfma_f32_16x16x32_f16 v[98:101], v[154:157], v[200:203], v[98:101]
	v_mfma_f32_16x16x32_f16 v[126:129], v[138:141], v[166:169], v[126:129]
	v_mfma_f32_16x16x32_f16 v[122:125], v[158:161], v[166:169], v[122:125]
	v_mfma_f32_16x16x32_f16 v[118:121], v[138:141], v[174:177], v[118:121]
	v_mfma_f32_16x16x32_f16 v[114:117], v[158:161], v[174:177], v[114:117]
	v_mfma_f32_16x16x32_f16 v[110:113], v[138:141], v[196:199], v[110:113]
	v_mfma_f32_16x16x32_f16 v[106:109], v[158:161], v[196:199], v[106:109]
	v_mfma_f32_16x16x32_f16 v[102:105], v[138:141], v[204:207], v[102:105]
	v_mfma_f32_16x16x32_f16 v[98:101], v[158:161], v[204:207], v[98:101]
	s_setprio 0
	s_barrier
	ds_read_b128 v[208:211], v163
	ds_read_b128 v[212:215], v163 offset:1024
	ds_read_b128 v[216:219], v163 offset:2048
	ds_read_b128 v[220:223], v163 offset:3072
	s_barrier
	s_waitcnt lgkmcnt(0)
	s_setprio 1
	s_waitcnt lgkmcnt(0)
	v_mfma_f32_16x16x32_f16 v[86:89], v[208:211], v[170:173], v[86:89]
	v_mfma_f32_16x16x32_f16 v[82:85], v[216:219], v[170:173], v[82:85]
	v_mfma_f32_16x16x32_f16 v[78:81], v[208:211], v[192:195], v[78:81]
	v_mfma_f32_16x16x32_f16 v[74:77], v[216:219], v[192:195], v[74:77]
	v_mfma_f32_16x16x32_f16 v[70:73], v[208:211], v[200:203], v[70:73]
	v_mfma_f32_16x16x32_f16 v[66:69], v[216:219], v[200:203], v[66:69]
	v_mfma_f32_16x16x32_f16 v[94:97], v[208:211], v[142:145], v[94:97]
	v_mfma_f32_16x16x32_f16 v[90:93], v[216:219], v[142:145], v[90:93]
	v_mfma_f32_16x16x32_f16 v[86:89], v[212:215], v[174:177], v[86:89]
	v_mfma_f32_16x16x32_f16 v[82:85], v[220:223], v[174:177], v[82:85]
	v_mfma_f32_16x16x32_f16 v[78:81], v[212:215], v[196:199], v[78:81]
	v_mfma_f32_16x16x32_f16 v[74:77], v[220:223], v[196:199], v[74:77]
	v_mfma_f32_16x16x32_f16 v[70:73], v[212:215], v[204:207], v[70:73]
	v_mfma_f32_16x16x32_f16 v[66:69], v[220:223], v[204:207], v[66:69]
	v_mfma_f32_16x16x32_f16 v[224:227], v[212:215], v[166:169], v[94:97]
	v_mfma_f32_16x16x32_f16 v[166:169], v[220:223], v[166:169], v[90:93]
	s_setprio 0
	s_barrier
	s_nop 0
	ds_read_b128 v[90:93], v150 offset:16384
	ds_read_b128 v[94:97], v150 offset:17408
	ds_read_b128 v[142:145], v149 offset:16384
	ds_read_b128 v[170:173], v149 offset:17408
	ds_read_b128 v[174:177], v148 offset:16384
	ds_read_b128 v[192:195], v148 offset:17408
	ds_read_b128 v[196:199], v147 offset:16384
	ds_read_b128 v[200:203], v147 offset:17408
	s_waitcnt vmcnt(4)
	s_barrier
	s_waitcnt lgkmcnt(0)
	s_setprio 1
	s_waitcnt lgkmcnt(0)
	v_mfma_f32_16x16x32_f16 v[62:65], v[134:137], v[90:93], v[62:65]
	v_mfma_f32_16x16x32_f16 v[58:61], v[154:157], v[90:93], v[58:61]
	v_mfma_f32_16x16x32_f16 v[54:57], v[134:137], v[142:145], v[54:57]
	v_mfma_f32_16x16x32_f16 v[50:53], v[154:157], v[142:145], v[50:53]
	v_mfma_f32_16x16x32_f16 v[46:49], v[134:137], v[174:177], v[46:49]
	v_mfma_f32_16x16x32_f16 v[42:45], v[154:157], v[174:177], v[42:45]
	v_mfma_f32_16x16x32_f16 v[38:41], v[134:137], v[196:199], v[38:41]
	v_mfma_f32_16x16x32_f16 v[62:65], v[138:141], v[94:97], v[62:65]
	v_mfma_f32_16x16x32_f16 v[58:61], v[158:161], v[94:97], v[58:61]
	v_mfma_f32_16x16x32_f16 v[54:57], v[138:141], v[170:173], v[54:57]
	v_mfma_f32_16x16x32_f16 v[50:53], v[158:161], v[170:173], v[50:53]
	v_mfma_f32_16x16x32_f16 v[46:49], v[138:141], v[192:195], v[46:49]
	v_mfma_f32_16x16x32_f16 v[42:45], v[158:161], v[192:195], v[42:45]
	v_mfma_f32_16x16x32_f16 v[38:41], v[138:141], v[200:203], v[38:41]
	v_mfma_f32_16x16x32_f16 v[34:37], v[154:157], v[196:199], v[34:37]
	v_mfma_f32_16x16x32_f16 v[34:37], v[158:161], v[200:203], v[34:37]
	s_setprio 0
	s_setprio 1
	v_mfma_f32_16x16x32_f16 v[30:33], v[208:211], v[90:93], v[30:33]
	v_mfma_f32_16x16x32_f16 v[6:9], v[208:211], v[196:199], v[6:9]
	v_mfma_f32_16x16x32_f16 v[2:5], v[216:219], v[196:199], v[2:5]
	v_mfma_f32_16x16x32_f16 v[30:33], v[212:215], v[94:97], v[30:33]
	v_mfma_f32_16x16x32_f16 v[26:29], v[216:219], v[90:93], v[26:29]
	v_mfma_f32_16x16x32_f16 v[22:25], v[208:211], v[142:145], v[22:25]
	v_mfma_f32_16x16x32_f16 v[18:21], v[216:219], v[142:145], v[18:21]
	v_mfma_f32_16x16x32_f16 v[14:17], v[208:211], v[174:177], v[14:17]
	v_mfma_f32_16x16x32_f16 v[10:13], v[216:219], v[174:177], v[10:13]
	v_mfma_f32_16x16x32_f16 v[6:9], v[212:215], v[200:203], v[6:9]
	v_mfma_f32_16x16x32_f16 v[2:5], v[220:223], v[200:203], v[2:5]
	v_mfma_f32_16x16x32_f16 v[26:29], v[220:223], v[94:97], v[26:29]
	v_mfma_f32_16x16x32_f16 v[154:157], v[212:215], v[170:173], v[22:25]
	v_mfma_f32_16x16x32_f16 v[18:21], v[220:223], v[170:173], v[18:21]
	v_mfma_f32_16x16x32_f16 v[158:161], v[212:215], v[192:195], v[14:17]
	v_mfma_f32_16x16x32_f16 v[10:13], v[220:223], v[192:195], v[10:13]
	s_setprio 0
	s_barrier
	ds_read_b128 v[14:17], v133
	ds_read_b128 v[22:25], v133 offset:1024
	ds_read_b128 v[170:173], v133 offset:2048
	ds_read_b128 v[174:177], v133 offset:3072
	ds_read_b128 v[192:195], v150 offset:32768
	ds_read_b128 v[196:199], v150 offset:33792
	ds_read_b128 v[200:203], v149 offset:32768
	ds_read_b128 v[204:207], v149 offset:33792
	ds_read_b128 v[208:211], v148 offset:32768
	ds_read_b128 v[212:215], v148 offset:33792
	ds_read_b128 v[216:219], v147 offset:32768
	ds_read_b128 v[220:223], v147 offset:33792
	s_waitcnt vmcnt(2)
	s_barrier
	s_waitcnt lgkmcnt(0)
	s_setprio 1
	s_waitcnt lgkmcnt(0)
	v_mfma_f32_16x16x32_f16 v[90:93], v[14:17], v[192:195], v[126:129]
	v_mfma_f32_16x16x32_f16 v[142:145], v[22:25], v[196:199], v[90:93]
	v_mfma_f32_16x16x32_f16 v[90:93], v[170:173], v[192:195], v[122:125]
	v_mfma_f32_16x16x32_f16 v[138:141], v[174:177], v[196:199], v[90:93]
	v_mfma_f32_16x16x32_f16 v[90:93], v[14:17], v[200:203], v[118:121]
	v_mfma_f32_16x16x32_f16 v[126:129], v[22:25], v[204:207], v[90:93]
	v_mfma_f32_16x16x32_f16 v[90:93], v[170:173], v[200:203], v[114:117]
	v_mfma_f32_16x16x32_f16 v[122:125], v[174:177], v[204:207], v[90:93]
	v_mfma_f32_16x16x32_f16 v[90:93], v[14:17], v[208:211], v[110:113]
	v_mfma_f32_16x16x32_f16 v[110:113], v[22:25], v[212:215], v[90:93]
	v_mfma_f32_16x16x32_f16 v[90:93], v[170:173], v[208:211], v[106:109]
	v_mfma_f32_16x16x32_f16 v[106:109], v[174:177], v[212:215], v[90:93]
	v_mfma_f32_16x16x32_f16 v[90:93], v[14:17], v[216:219], v[102:105]
	v_mfma_f32_16x16x32_f16 v[94:97], v[22:25], v[220:223], v[90:93]
	v_mfma_f32_16x16x32_f16 v[90:93], v[170:173], v[216:219], v[98:101]
	v_mfma_f32_16x16x32_f16 v[90:93], v[174:177], v[220:223], v[90:93]
	s_setprio 0
	s_barrier
	ds_read_b128 v[228:231], v131
	ds_read_b128 v[232:235], v131 offset:1024
	ds_read_b128 v[236:239], v131 offset:2048
	ds_read_b128 v[240:243], v131 offset:3072
	s_waitcnt vmcnt(0)
	s_barrier
	s_waitcnt lgkmcnt(0)
	s_setprio 1
	s_waitcnt lgkmcnt(0)
	v_mfma_f32_16x16x32_f16 v[98:101], v[228:231], v[192:195], v[224:227]
	v_mfma_f32_16x16x32_f16 v[134:137], v[232:235], v[196:199], v[98:101]
	v_mfma_f32_16x16x32_f16 v[98:101], v[236:239], v[192:195], v[166:169]
	v_mfma_f32_16x16x32_f16 v[86:89], v[228:231], v[200:203], v[86:89]
	v_mfma_f32_16x16x32_f16 v[82:85], v[236:239], v[200:203], v[82:85]
	v_mfma_f32_16x16x32_f16 v[78:81], v[228:231], v[208:211], v[78:81]
	v_mfma_f32_16x16x32_f16 v[74:77], v[236:239], v[208:211], v[74:77]
	v_mfma_f32_16x16x32_f16 v[70:73], v[228:231], v[216:219], v[70:73]
	v_mfma_f32_16x16x32_f16 v[66:69], v[236:239], v[216:219], v[66:69]
	v_mfma_f32_16x16x32_f16 v[130:133], v[240:243], v[196:199], v[98:101]
	v_mfma_f32_16x16x32_f16 v[118:121], v[232:235], v[204:207], v[86:89]
	v_mfma_f32_16x16x32_f16 v[114:117], v[240:243], v[204:207], v[82:85]
	v_mfma_f32_16x16x32_f16 v[102:105], v[232:235], v[212:215], v[78:81]
	v_mfma_f32_16x16x32_f16 v[98:101], v[240:243], v[212:215], v[74:77]
	v_mfma_f32_16x16x32_f16 v[86:89], v[232:235], v[220:223], v[70:73]
	v_mfma_f32_16x16x32_f16 v[82:85], v[240:243], v[220:223], v[66:69]
	s_setprio 0
	s_barrier
	s_nop 0
	ds_read_b128 v[66:69], v150 offset:49152
	ds_read_b128 v[166:169], v150 offset:50176
	ds_read_b128 v[192:195], v149 offset:49152
	ds_read_b128 v[196:199], v149 offset:50176
	ds_read_b128 v[200:203], v148 offset:49152
	ds_read_b128 v[148:151], v148 offset:50176
	ds_read_b128 v[204:207], v147 offset:49152
	ds_read_b128 v[208:211], v147 offset:50176
	s_barrier
	s_waitcnt lgkmcnt(0)
	s_setprio 1
	s_waitcnt lgkmcnt(0)
	v_mfma_f32_16x16x32_f16 v[62:65], v[14:17], v[66:69], v[62:65]
	v_mfma_f32_16x16x32_f16 v[54:57], v[14:17], v[192:195], v[54:57]
	v_mfma_f32_16x16x32_f16 v[46:49], v[14:17], v[200:203], v[46:49]
	v_mfma_f32_16x16x32_f16 v[14:17], v[14:17], v[204:207], v[38:41]
	v_mfma_f32_16x16x32_f16 v[78:81], v[22:25], v[166:169], v[62:65]
	v_mfma_f32_16x16x32_f16 v[58:61], v[170:173], v[66:69], v[58:61]
	v_mfma_f32_16x16x32_f16 v[62:65], v[22:25], v[196:199], v[54:57]
	v_mfma_f32_16x16x32_f16 v[50:53], v[170:173], v[192:195], v[50:53]
	v_mfma_f32_16x16x32_f16 v[46:49], v[22:25], v[148:151], v[46:49]
	v_mfma_f32_16x16x32_f16 v[42:45], v[170:173], v[200:203], v[42:45]
	v_mfma_f32_16x16x32_f16 v[22:25], v[22:25], v[208:211], v[14:17]
	v_mfma_f32_16x16x32_f16 v[14:17], v[170:173], v[204:207], v[34:37]
	v_mfma_f32_16x16x32_f16 v[74:77], v[174:177], v[166:169], v[58:61]
	v_mfma_f32_16x16x32_f16 v[58:61], v[174:177], v[196:199], v[50:53]
	v_mfma_f32_16x16x32_f16 v[42:45], v[174:177], v[148:151], v[42:45]
	v_mfma_f32_16x16x32_f16 v[14:17], v[174:177], v[208:211], v[14:17]
	s_setprio 0
	s_setprio 1
	v_mfma_f32_16x16x32_f16 v[26:29], v[236:239], v[66:69], v[26:29]
	v_mfma_f32_16x16x32_f16 v[18:21], v[236:239], v[192:195], v[18:21]
	v_mfma_f32_16x16x32_f16 v[30:33], v[228:231], v[66:69], v[30:33]
	v_mfma_f32_16x16x32_f16 v[66:69], v[240:243], v[166:169], v[26:29]
	v_mfma_f32_16x16x32_f16 v[26:29], v[228:231], v[192:195], v[154:157]
	v_mfma_f32_16x16x32_f16 v[50:53], v[240:243], v[196:199], v[18:21]
	v_mfma_f32_16x16x32_f16 v[18:21], v[228:231], v[200:203], v[158:161]
	v_mfma_f32_16x16x32_f16 v[10:13], v[236:239], v[200:203], v[10:13]
	v_mfma_f32_16x16x32_f16 v[6:9], v[228:231], v[204:207], v[6:9]
	v_mfma_f32_16x16x32_f16 v[2:5], v[236:239], v[204:207], v[2:5]
	v_mfma_f32_16x16x32_f16 v[70:73], v[232:235], v[166:169], v[30:33]
	v_mfma_f32_16x16x32_f16 v[54:57], v[232:235], v[196:199], v[26:29]
	v_mfma_f32_16x16x32_f16 v[38:41], v[232:235], v[148:151], v[18:21]
	v_mfma_f32_16x16x32_f16 v[30:33], v[240:243], v[148:151], v[10:13]
	v_mfma_f32_16x16x32_f16 v[6:9], v[232:235], v[208:211], v[6:9]
	v_mfma_f32_16x16x32_f16 v[2:5], v[240:243], v[208:211], v[2:5]
	s_setprio 0
	s_movk_i32 s0, 0x100
	v_cmp_gt_u32_e32 vcc, s0, v0
	s_barrier
	s_and_saveexec_b64 s[0:1], vcc
	s_cbranch_execz .LBB5_12
	s_barrier
